# P4 prep: token's PROJ loads + position load issued one token ahead (second register set); in-body dependent position round trip and drained waits removed
# baseline (speedup 1.0000x reference)
; __device__ __forceinline__ void p3_prep(Frame& F) {
;     const int gw = F.bid * NWAVES + F.wave, NGW = F.G * NWAVES, lane = F.lane;
;     for (int t = gw; t < S_; t += NGW) {
;         const bf16_t* pr = WSP(bf16_t, WS_PROJ) + (size_t)t * D_INP;
;         { const u32x4 w = *(const u32x4*)(pr + 3072 + 8 * lane); float s = 0.f;
; #pragma unroll
;           for (int i = 0; i < 4; ++i) { const float a = bf_lo(w[i]), b = bf_hi(w[i]); s += a * a + b * b; }
;           s = wave_sum(s); if (lane == 0) WSP(float, WS_RQ)[t] = 1.f / sqrtf(s * (1.f / 512.f) + EPS_); }
;         { float s = 0.f; if (lane < 32) { const u32x4 w = *(const u32x4*)(pr + 3584 + 8 * lane);
; #pragma unroll
;               for (int i = 0; i < 4; ++i) { const float a = bf_lo(w[i]), b = bf_hi(w[i]); s += a * a + b * b; } }
;           s = wave_sum(s); if (lane == 0) WSP(float, WS_RKV)[t] = 1.f / sqrtf(s * (1.f / 256.f) + EPS_); }
;         if (lane < 32) {
;             const float x1 = __builtin_bit_cast(float, (unsigned)pr[3840 + lane] << 16), x2 = __builtin_bit_cast(float, (unsigned)pr[3872 + lane] << 16);
;             const float inv = powf(10000.f, -(float)lane / 32.f); const float ang = (float)INI(I_POS)[t] * inv;
.LBB0_336:
	s_cmp_lt_i32 s28, 5
	s_cselect_b64 s[6:7], -1, 0
	s_and_b64 s[14:15], s[6:7], s[4:5]
	s_andn2_b64 vcc, exec, s[14:15]
	s_cbranch_vccnz .LBB0_352
	v_mov_b32_e32 v1, v0
	s_lshl_b32 s4, s2, 3
	v_readfirstlane_b32 s5, v1
	s_ashr_i32 s5, s5, 6
	s_add_i32 s18, s5, s4
	s_mov_b64 s[16:17], s[0:1]
	s_cmpk_gt_i32 s18, 0x3fff
	s_cbranch_scc1 .LBB0_352
	v_and_b32_e32 v22, 63, v1
	v_mbcnt_lo_u32_b32 v1, -1, 0
	v_mbcnt_hi_u32_b32 v2, -1, v1
	v_and_b32_e32 v1, 64, v2
	v_add_u32_e32 v3, 64, v1
	v_xor_b32_e32 v1, 1, v2
	v_cmp_lt_i32_e32 vcc, v1, v3
	v_xor_b32_e32 v4, 2, v2
	s_mov_b32 s8, 0x3f2aaaab
	v_cndmask_b32_e32 v1, v2, v1, vcc
	v_cmp_lt_i32_e32 vcc, v4, v3
	s_waitcnt lgkmcnt(0)
	s_movk_i32 s10, 0x204
	s_mov_b32 s12, 0x42b17218
	v_cndmask_b32_e32 v4, v2, v4, vcc
	v_lshlrev_b32_e32 v14, 2, v4
	v_xor_b32_e32 v4, 4, v2
	v_cmp_lt_i32_e32 vcc, v4, v3
	s_mov_b32 s11, 0x7f800000
	s_load_dwordx2 s[22:23], s[16:17], 0xc8
	v_cndmask_b32_e32 v4, v2, v4, vcc
	v_lshlrev_b32_e32 v15, 2, v4
	v_xor_b32_e32 v4, 8, v2
	v_cmp_lt_i32_e32 vcc, v4, v3
	s_ashr_i32 s19, s18, 31
	s_ashr_i32 s27, s26, 31
	v_cndmask_b32_e32 v4, v2, v4, vcc
	v_lshlrev_b32_e32 v16, 2, v4
	v_xor_b32_e32 v4, 16, v2
	v_cmp_lt_i32_e32 vcc, v4, v3
	v_lshlrev_b32_e32 v1, 2, v1
	v_cmp_eq_u32_e64 s[4:5], 0, v22
	v_cndmask_b32_e32 v4, v2, v4, vcc
	v_lshlrev_b32_e32 v17, 2, v4
	v_xor_b32_e32 v4, 32, v2
	v_cmp_lt_i32_e32 vcc, v4, v3
	v_cmp_gt_u32_e64 s[6:7], 32, v22
	s_lshl_b64 s[24:25], s[18:19], 2
	v_cndmask_b32_e32 v2, v2, v4, vcc
	v_lshlrev_b32_e32 v18, 2, v2
	v_cvt_f32_ubyte0_e32 v2, v22
	v_mul_f32_e32 v19, 0xbd000000, v2
	v_mov_b32_e32 v2, 0x461c4000
	v_cmp_eq_f32_e32 vcc, 0, v19
	s_lshl_b64 s[38:39], s[26:27], 2
	s_lshl_b64 s[40:41], s[26:27], 7
	v_cndmask_b32_e64 v12, v2, 1.0, vcc
	v_frexp_mant_f32_e32 v2, v12
	v_cmp_gt_f32_e64 s[8:9], s8, v2
	s_lshl_b64 s[42:43], s[26:27], 13
	v_mov_b32_e32 v23, 0x130000
	v_cndmask_b32_e64 v3, 1.0, 2.0, s[8:9]
	v_mul_f32_e32 v2, v2, v3
	v_add_f32_e32 v5, 1.0, v2
	v_rcp_f32_e32 v10, v5
	v_add_f32_e32 v3, -1.0, v5
	v_sub_f32_e32 v7, v2, v3
	v_add_f32_e32 v3, -1.0, v2
	v_mul_f32_e32 v11, v3, v10
	v_mul_f32_e32 v4, v5, v11
	v_fma_f32 v6, v11, v5, -v4
	v_fmac_f32_e32 v6, v11, v7
	v_add_f32_e32 v2, v4, v6
	v_sub_f32_e32 v5, v3, v2
	v_pk_add_f32 v[8:9], v[2:3], v[4:5] neg_lo:[0,1] neg_hi:[0,1]
	v_mov_b32_e32 v7, v2
	v_pk_add_f32 v[2:3], v[8:9], v[6:7] neg_lo:[0,1] neg_hi:[0,1]
	v_mov_b32_e32 v6, 0x3e91f4c4
	v_add_f32_e32 v2, v2, v3
	v_add_f32_e32 v2, v5, v2
	v_mul_f32_e32 v3, v10, v2
	v_add_f32_e32 v2, v11, v3
	v_sub_f32_e32 v4, v2, v11
	v_sub_f32_e32 v13, v3, v4
	v_mul_f32_e32 v3, v2, v2
	v_fma_f32 v5, v2, v2, -v3
	v_add_f32_e32 v4, v13, v13
	v_fmac_f32_e32 v5, v2, v4
	v_add_f32_e32 v4, v3, v5
	v_fmac_f32_e32 v6, 0x3e76c4e1, v4
	v_fmaak_f32 v6, v4, v6, 0x3ecccdef
	v_sub_f32_e32 v3, v4, v3
	v_sub_f32_e32 v20, v5, v3
	v_mul_f32_e32 v3, v4, v6
	v_fma_f32 v5, v4, v6, -v3
	v_fmac_f32_e32 v5, v20, v6
	v_add_f32_e32 v6, v3, v5
	v_add_f32_e32 v7, 0x3f2aaaaa, v6
	v_sub_f32_e32 v3, v6, v3
	v_sub_f32_e32 v3, v5, v3
	v_add_f32_e32 v5, 0xbf2aaaaa, v7
	v_add_f32_e32 v3, 0x31739010, v3
	v_sub_f32_e32 v5, v6, v5
	v_pk_mul_f32 v[8:9], v[2:3], v[4:5]
	v_pk_add_f32 v[10:11], v[2:3], v[4:5]
	v_fma_f32 v6, v4, v2, -v8
	v_fmac_f32_e32 v6, v4, v13
	v_mov_b32_e32 v9, v11
	v_fmac_f32_e32 v6, v20, v2
	v_pk_add_f32 v[4:5], v[8:9], v[6:7]
	v_ldexp_f32 v20, v13, 1
	v_sub_f32_e32 v3, v4, v8
	v_sub_f32_e32 v3, v6, v3
	v_sub_f32_e32 v6, v7, v5
	v_add_f32_e32 v9, v11, v6
	v_pk_mul_f32 v[6:7], v[4:5], v[4:5] op_sel:[0,1] op_sel_hi:[1,0]
	v_cvt_f64_f32_e32 v[10:11], v12
	v_frexp_exp_i32_f64_e32 v7, v[10:11]
	v_subbrev_co_u32_e64 v7, s[8:9], 0, v7, s[8:9]
	v_cvt_f32_i32_e32 v7, v7
	v_fma_f32 v8, v4, v5, -v6
	v_fmac_f32_e32 v8, v4, v9
	s_mov_b32 s8, 0x3f317218
	v_mul_f32_e32 v4, 0x3f317218, v7
	v_fmac_f32_e32 v8, v3, v5
	v_fma_f32 v3, v7, s8, -v4
	v_fmamk_f32 v10, v7, 0xb102e308, v3
	v_ldexp_f32 v11, v2, 1
	v_add_f32_e32 v5, v6, v8
	v_pk_add_f32 v[2:3], v[4:5], v[10:11]
	v_mov_b32_e32 v12, v5
	v_mov_b32_e32 v13, v3
	v_mov_b32_e32 v7, v11
	v_pk_add_f32 v[6:7], v[12:13], v[6:7] neg_lo:[0,1] neg_hi:[0,1]
	v_mov_b32_e32 v9, v5
	v_pk_add_f32 v[6:7], v[8:9], v[6:7] neg_lo:[0,1] neg_hi:[0,1]
	v_mov_b32_e32 v11, v2
	v_add_f32_e32 v5, v20, v6
	v_add_f32_e32 v5, v5, v7
	v_pk_add_f32 v[6:7], v[2:3], v[4:5] neg_lo:[0,1] neg_hi:[0,1]
	v_pk_add_f32 v[8:9], v[2:3], v[4:5]
	v_mov_b32_e32 v4, v5
	v_mov_b32_e32 v7, v9
	v_pk_add_f32 v[12:13], v[10:11], v[6:7] neg_lo:[0,1] neg_hi:[0,1]
	v_pk_add_f32 v[6:7], v[10:11], v[6:7]
	v_mov_b32_e32 v5, v2
	v_pk_add_f32 v[10:11], v[6:7], v[2:3] op_sel:[1,0] op_sel_hi:[0,1] neg_lo:[0,1] neg_hi:[0,1]
	v_pk_add_f32 v[20:21], v[8:9], v[10:11] op_sel_hi:[1,0] neg_lo:[0,1] neg_hi:[0,1]
	v_mov_b32_e32 v8, v9
	v_mov_b32_e32 v9, v7
	v_pk_mov_b32 v[10:11], v[2:3], v[10:11] op_sel:[1,0]
	v_mov_b32_e32 v20, v12
	v_pk_add_f32 v[8:9], v[8:9], v[10:11] neg_lo:[0,1] neg_hi:[0,1]
	v_mov_b32_e32 v13, v7
	v_pk_add_f32 v[2:3], v[4:5], v[8:9] neg_lo:[0,1] neg_hi:[0,1]
	s_brev_b32 s27, 18
	v_pk_add_f32 v[4:5], v[20:21], v[2:3]
; __device__ __forceinline__ unsigned f2bf(float f) { unsigned u = __builtin_bit_cast(unsigned, f); return (u + 0x7fffu + ((u >> 16) & 1u)) >> 16; }
; __device__ __forceinline__ void p3_prep(Frame& F) {
;     ...
;             const float inv = powf(10000.f, -(float)lane / 32.f); const float ang = (float)INI(I_POS)[t] * inv;
;             float sn, cs; sincosf(ang, &sn, &cs);
;             WSP(float, WS_COS)[(size_t)t * 32 + lane] = cs; WSP(float, WS_SIN)[(size_t)t * 32 + lane] = sn;
;             bf16_t* kr = WSP(bf16_t, WS_KR) + (size_t)t * 64;
;             kr[lane] = (bf16_t)f2bf(x1 * cs - x2 * sn); kr[32 + lane] = (bf16_t)f2bf(x2 * cs + x1 * sn);
	v_mov_b32_e32 v20, 0x358637bd
	v_pk_add_f32 v[8:9], v[4:5], v[4:5] op_sel:[0,1] op_sel_hi:[1,0]
	v_mov_b32_e32 v21, 0x260
	v_pk_add_f32 v[6:7], v[6:7], v[8:9] op_sel:[1,0] op_sel_hi:[0,1]
	v_mov_b32_e32 v5, v6
	v_pk_add_f32 v[10:11], v[4:5], v[12:13] neg_lo:[0,1] neg_hi:[0,1]
	v_mov_b32_e32 v3, v8
	v_sub_f32_e32 v4, v4, v10
	v_pk_add_f32 v[2:3], v[2:3], v[10:11] neg_lo:[0,1] neg_hi:[0,1]
	v_sub_f32_e32 v4, v12, v4
	v_add_f32_e32 v2, v2, v4
	v_add_f32_e32 v2, v2, v3
	v_add_f32_e32 v3, v6, v2
	v_sub_f32_e32 v4, v3, v6
	v_sub_f32_e32 v2, v2, v4
	v_mul_f32_e32 v4, v19, v3
	v_fma_f32 v3, v19, v3, -v4
	v_fmac_f32_e32 v3, v19, v2
	v_add_f32_e32 v2, v4, v3
	v_cmp_class_f32_e64 s[8:9], v4, s10
	v_sub_f32_e32 v5, v2, v4
	v_sub_f32_e32 v3, v3, v5
	v_cndmask_b32_e64 v2, v2, v4, s[8:9]
	v_mov_b32_e32 v4, 0x37000000
	v_cmp_eq_f32_e64 s[8:9], s12, v2
	v_lshlrev_b32_e32 v10, 1, v22
	s_mov_b32 s36, 0xfe5163ab
	v_cndmask_b32_e64 v4, 0, v4, s[8:9]
	v_sub_f32_e32 v5, v2, v4
	s_mov_b32 s8, 0x3fb8aa3b
	v_mul_f32_e32 v6, 0x3fb8aa3b, v5
	v_fma_f32 v7, v5, s8, -v6
	v_rndne_f32_e32 v8, v6
	v_fmamk_f32 v7, v5, 0x32a5705f, v7
	v_sub_f32_e32 v6, v6, v8
	v_add_f32_e32 v6, v6, v7
	v_exp_f32_e32 v6, v6
	v_cvt_i32_f32_e32 v7, v8
	v_cmp_neq_f32_e64 s[8:9], |v2|, s11
	s_mov_b32 s37, 0x3c439041
	s_mov_b32 s48, 0xdb629599
	v_cndmask_b32_e64 v2, 0, v3, s[8:9]
	s_mov_b32 s8, 0xc2ce8ed0
	v_ldexp_f32 v3, v6, v7
	v_cmp_ngt_f32_e64 s[8:9], s8, v5
	v_add_f32_e32 v2, v4, v2
	v_mov_b32_e32 v4, 0x7f800000
	v_cndmask_b32_e64 v3, 0, v3, s[8:9]
	v_cmp_nlt_f32_e64 s[8:9], s12, v5
	v_mov_b32_e32 v5, 0
	s_mov_b32 s49, 0xf534ddc0
	v_cndmask_b32_e64 v3, v4, v3, s[8:9]
	v_fma_f32 v2, v3, v2, v3
	v_cmp_class_f32_e64 s[8:9], v3, s10
	s_mov_b32 s50, 0xfc2757d1
	s_mov_b32 s51, 0x4e441529
	v_cndmask_b32_e64 v2, v2, v3, s[8:9]
	v_cmp_neq_f32_e64 s[8:9], v19, |v19|
	s_mov_b32 s52, 0xa2f9836e
	s_mov_b32 s53, 0x3fc90fda
	v_cndmask_b32_e64 v3, v4, 0, s[8:9]
	v_cndmask_b32_e64 v3, v3, 1.0, vcc
	v_cmp_class_f32_e64 s[8:9], v19, s10
	v_lshlrev_b32_e32 v4, 2, v22
	s_mov_b32 s54, 0x3f22f983
	v_cndmask_b32_e64 v19, |v2|, v3, s[8:9]
	s_lshl_b64 s[8:9], s[18:19], 7
	v_or_b32_e32 v2, s8, v10
	v_mov_b32_e32 v3, s9
	v_lshl_add_u64 v[6:7], s[8:9], 0, v[4:5]
	s_lshl_b64 s[8:9], s[18:19], 13
	v_lshl_or_b32 v8, v22, 4, s8
	v_mov_b32_e32 v9, s9
	v_or_b32_e32 v10, s8, v10
	v_mov_b32_e32 v11, s9
	s_mov_b32 s19, 0xf800000
	v_mov_b32_e32 v22, 0x120000
	s_mov_b32 s55, 0xbfc90fda
	v_mov_b32_e32 v24, 0x3c0881c4
	v_mov_b32_e32 v25, 0xbab64f3b
	s_brev_b32 s56, 1
	s_movk_i32 s57, 0x1f8
	s_mov_b32 s58, 0x400000
	s_movk_i32 s59, 0x7fff
	v_not_b32_e32 v26, 63
	v_not_b32_e32 v27, 31
	v_mov_b32_e32 v28, 0x7fc00000
	v_lshl_add_u64 v[122:123], s[22:23], 0, v[8:9]
	v_add_co_u32_e32 v122, vcc, 0x1f701000, v122
	s_nop 1
	v_addc_co_u32_e32 v123, vcc, 0, v123, vcc
	global_load_dwordx4 v[110:113], v[122:123], off offset:3072
	global_load_dwordx4 v[114:117], v[122:123], off offset:2048
	v_lshl_add_u64 v[124:125], s[22:23], 0, v[10:11]
	v_add_co_u32_e32 v124, vcc, 0x1f701000, v124
	s_nop 1
	v_addc_co_u32_e32 v125, vcc, 0, v125, vcc
	global_load_ushort v118, v[124:125], off offset:3584
	global_load_ushort v119, v[124:125], off offset:3648
	s_load_dwordx2 s[8:9], s[16:17], 0x10
	v_mov_b32_e32 v121, 0
	s_waitcnt lgkmcnt(0)
	s_add_u32 s8, s8, s24
	s_addc_u32 s9, s9, s25
	global_load_dword v120, v121, s[8:9]
	s_branch .LBB0_341
.LBB0_339:
	s_or_b64 exec, exec, s[8:9]
	v_lshlrev_b32_e32 v32, 16, v107
	v_mul_f32_e32 v30, v4, v4
	v_fmamk_f32 v33, v30, 0xb94c1982, v24
	v_fmaak_f32 v33, v30, v33, 0xbe2aaa9d
	v_mul_f32_e32 v33, v30, v33
	v_fmac_f32_e32 v4, v4, v33
	v_fmamk_f32 v33, v30, 0x37d75334, v25
	v_fmaak_f32 v33, v30, v33, 0x3d2aabf7
	v_fmaak_f32 v33, v30, v33, 0xbf000004
	v_fma_f32 v30, v30, v33, 1.0
	v_lshlrev_b32_e32 v33, 30, v31
	v_and_b32_e32 v31, 1, v31
	v_cmp_eq_u32_e32 vcc, 0, v31
	v_xor_b32_e32 v13, v13, v12
	v_and_b32_e32 v34, 0x80000000, v33
	v_cndmask_b32_e32 v31, v30, v4, vcc
	v_xor_b32_e32 v13, v13, v31
	v_xor_b32_e32 v4, 0x80000000, v4
	v_xor_b32_e32 v13, v13, v34
	v_cndmask_b32_e32 v4, v4, v30, vcc
	v_cmp_class_f32_e64 vcc, v12, s57
	v_bitop3_b32 v4, v4, v33, s56 bitop3:0x78
	v_lshlrev_b32_e32 v29, 16, v106
	v_cndmask_b32_e32 v33, v28, v13, vcc
	v_lshl_add_u64 v[12:13], s[22:23], 0, v[6:7]
	v_cndmask_b32_e32 v4, v28, v4, vcc
	v_add_co_u32_e32 v30, vcc, s58, v12
	s_nop 1
	v_addc_co_u32_e32 v31, vcc, 0, v13, vcc
	v_add_co_u32_e32 v12, vcc, 0x600000, v12
	global_store_dword v[30:31], v4, off
	s_nop 0
	v_addc_co_u32_e32 v13, vcc, 0, v13, vcc
	global_store_dword v[12:13], v33, off
	v_mul_f32_e32 v12, v33, v32
	v_fma_f32 v12, v4, v29, -v12
	v_bfe_u32 v13, v12, 16, 1
	v_mul_f32_e32 v29, v33, v29
	v_add3_u32 v30, v12, v13, s59
	v_lshl_add_u64 v[12:13], s[22:23], 0, v[2:3]
	v_fmac_f32_e32 v29, v4, v32
	v_add_co_u32_e32 v12, vcc, 0x800000, v12
	v_bfe_u32 v4, v29, 16, 1
	s_nop 0
	v_addc_co_u32_e32 v13, vcc, 0, v13, vcc
	v_add3_u32 v4, v29, v4, s59
	global_store_short_d16_hi v[12:13], v30, off
	global_store_short_d16_hi v[12:13], v4, off offset:64

; __device__ __forceinline__ void p3_prep(Frame& F) {
;     ...
;     for (int t = gw; t < S_; t += NGW) {
;         const bf16_t* pr = WSP(bf16_t, WS_PROJ) + (size_t)t * D_INP;
;         { const u32x4 w = *(const u32x4*)(pr + 3072 + 8 * lane); float s = 0.f;
; #pragma unroll
;           for (int i = 0; i < 4; ++i) { const float a = bf_lo(w[i]), b = bf_hi(w[i]); s += a * a + b * b; }
;           s = wave_sum(s); if (lane == 0) WSP(float, WS_RQ)[t] = 1.f / sqrtf(s * (1.f / 512.f) + EPS_); }
.LBB0_341:
	s_waitcnt lgkmcnt(0)
	v_lshl_add_u64 v[12:13], s[22:23], 0, v[8:9]
	v_add_co_u32_e32 v30, vcc, 0x1f701000, v12
	s_nop 1
	v_addc_co_u32_e32 v31, vcc, 0, v13, vcc
	v_lshl_add_u64 v[104:105], s[22:23], 0, v[10:11]
	v_add_co_u32_e32 v104, vcc, 0x1f701000, v104
	s_nop 1
	v_addc_co_u32_e32 v105, vcc, 0, v105, vcc
	s_waitcnt vmcnt(0)
	v_mov_b32_e32 v100, v110
	v_mov_b32_e32 v101, v111
	v_mov_b32_e32 v102, v112
	v_mov_b32_e32 v103, v113
	v_mov_b32_e32 v30, v114
	v_mov_b32_e32 v31, v115
	v_mov_b32_e32 v32, v116
	v_mov_b32_e32 v33, v117
	v_mov_b32_e32 v106, v118
	v_mov_b32_e32 v107, v119
	v_mov_b32_e32 v109, v120
	s_add_i32 s8, s18, s26
	s_cmpk_lt_i32 s8, 0x4000
	s_cbranch_scc0 .Lmy_p4_nopf
	v_lshl_add_u64 v[122:123], v[8:9], 0, s[42:43]
	v_lshl_add_u64 v[122:123], s[22:23], 0, v[122:123]
	v_add_co_u32_e32 v122, vcc, 0x1f701000, v122
	s_nop 1
	v_addc_co_u32_e32 v123, vcc, 0, v123, vcc
	global_load_dwordx4 v[110:113], v[122:123], off offset:3072
	global_load_dwordx4 v[114:117], v[122:123], off offset:2048
	v_lshl_add_u64 v[124:125], v[10:11], 0, s[42:43]
	v_lshl_add_u64 v[124:125], s[22:23], 0, v[124:125]
	v_add_co_u32_e32 v124, vcc, 0x1f701000, v124
	s_nop 1
	v_addc_co_u32_e32 v125, vcc, 0, v125, vcc
	global_load_ushort v118, v[124:125], off offset:3584
	global_load_ushort v119, v[124:125], off offset:3648
	s_load_dwordx2 s[8:9], s[16:17], 0x10
	v_mov_b32_e32 v121, 0
	s_waitcnt lgkmcnt(0)
	s_add_u32 s8, s8, s24
	s_addc_u32 s9, s9, s25
	s_add_u32 s8, s8, s38
	s_addc_u32 s9, s9, s39
	global_load_dword v120, v121, s[8:9]
.Lmy_p4_nopf:
	v_lshlrev_b32_e32 v4, 16, v30
	v_and_b32_e32 v29, 0xffff0000, v30
	v_lshlrev_b32_e32 v30, 16, v31
	v_and_b32_e32 v31, 0xffff0000, v31
	v_lshlrev_b32_e32 v34, 16, v32
	v_and_b32_e32 v32, 0xffff0000, v32
	v_mul_f32_e32 v29, v29, v29
	v_mul_f32_e32 v31, v31, v31
	v_lshlrev_b32_e32 v35, 16, v33
	v_and_b32_e32 v33, 0xffff0000, v33
	v_mul_f32_e32 v32, v32, v32
	v_fmac_f32_e32 v29, v4, v4
	v_fmac_f32_e32 v31, v30, v30
	v_mul_f32_e32 v33, v33, v33
	v_fmac_f32_e32 v32, v34, v34
	v_add_f32_e32 v4, v29, v31
	v_add_f32_e32 v4, v32, v4
	v_fmac_f32_e32 v33, v35, v35
	v_add_f32_e32 v4, v33, v4
	s_waitcnt lgkmcnt(0)
	s_nop 1
	v_add_f32_dpp v4, v4, v4 quad_perm:[1,0,3,2] row_mask:0xf bank_mask:0xf bound_ctrl:1
	s_waitcnt lgkmcnt(0)
	s_nop 1
	v_add_f32_dpp v4, v4, v4 quad_perm:[2,3,0,1] row_mask:0xf bank_mask:0xf bound_ctrl:1
	s_waitcnt lgkmcnt(0)
	s_nop 1
	v_add_f32_dpp v4, v4, v4 row_half_mirror row_mask:0xf bank_mask:0xf bound_ctrl:1
	s_waitcnt lgkmcnt(0)
	s_nop 1
	v_add_f32_dpp v4, v4, v4 row_mirror row_mask:0xf bank_mask:0xf bound_ctrl:1
	ds_bpermute_b32 v29, v17, v4
	s_waitcnt lgkmcnt(0)
	v_add_f32_e32 v4, v4, v29
	ds_bpermute_b32 v29, v18, v4
	s_and_saveexec_b64 s[10:11], s[4:5]
	s_cbranch_execz .LBB0_343
	s_waitcnt lgkmcnt(0)
	v_add_f32_e32 v4, v4, v29
	v_fmamk_f32 v4, v4, 0x3b000000, v20
	v_mul_f32_e32 v29, 0x4f800000, v4
	v_cmp_gt_f32_e32 vcc, s19, v4
	s_nop 1
	v_cndmask_b32_e32 v4, v4, v29, vcc
	v_sqrt_f32_e32 v29, v4
	s_nop 0
	v_add_u32_e32 v30, -1, v29
	v_fma_f32 v32, -v30, v29, v4
	v_add_u32_e32 v31, 1, v29
	v_cmp_ge_f32_e64 s[8:9], 0, v32
	s_nop 1
	v_cndmask_b32_e64 v30, v29, v30, s[8:9]
	v_fma_f32 v29, -v31, v29, v4
	v_cmp_lt_f32_e64 s[8:9], 0, v29
	s_nop 1
	v_cndmask_b32_e64 v29, v30, v31, s[8:9]
	v_mul_f32_e32 v30, 0x37800000, v29
	v_cndmask_b32_e32 v29, v29, v30, vcc
	v_cmp_class_f32_e32 vcc, v4, v21
	s_nop 1
	v_cndmask_b32_e32 v4, v29, v4, vcc
	v_div_scale_f32 v29, s[8:9], v4, v4, 1.0
	v_rcp_f32_e32 v30, v29
	s_add_u32 s8, s22, s24
	s_addc_u32 s9, s23, s25
	v_fma_f32 v31, -v29, v30, 1.0
	v_fmac_f32_e32 v30, v31, v30
	v_div_scale_f32 v31, vcc, 1.0, v4, 1.0
	v_mul_f32_e32 v32, v31, v30
	v_fma_f32 v33, -v29, v32, v31
	v_fmac_f32_e32 v32, v33, v30
	v_fma_f32 v29, -v29, v32, v31
	v_div_fmas_f32 v29, v29, v30, v32
	v_div_fixup_f32 v4, v29, v4, 1.0
	global_store_dword v22, v4, s[8:9]

; __device__ __forceinline__ void p3_prep(Frame& F) {
;     ...
;         if (lane < 32) {
;             const float x1 = __builtin_bit_cast(float, (unsigned)pr[3840 + lane] << 16), x2 = __builtin_bit_cast(float, (unsigned)pr[3872 + lane] << 16);
;             const float inv = powf(10000.f, -(float)lane / 32.f); const float ang = (float)INI(I_POS)[t] * inv;
;             float sn, cs; sincosf(ang, &sn, &cs);
.LBB0_347:
	s_or_b64 exec, exec, s[10:11]
	s_and_saveexec_b64 s[44:45], s[6:7]
	s_cbranch_execz .LBB0_340
	s_waitcnt lgkmcnt(0)
	v_lshl_add_u64 v[12:13], s[22:23], 0, v[10:11]
	v_add_co_u32_e32 v12, vcc, 0x1f701000, v12
	v_mov_b32_e32 v4, v109
	v_addc_co_u32_e32 v13, vcc, 0, v13, vcc
	v_cvt_f32_i32_e32 v4, v4
	v_mul_f32_e32 v12, v19, v4
	v_and_b32_e32 v13, 0x7fffffff, v12
	v_cmp_nlt_f32_e64 s[8:9], |v12|, s27
	s_and_saveexec_b64 s[10:11], s[8:9]
	s_xor_b64 s[46:47], exec, s[10:11]
	s_cbranch_execz .LBB0_350
	v_lshrrev_b32_e32 v4, 23, v13
	v_add_u32_e32 v4, 0xffffff88, v4
	v_cmp_lt_u32_e32 vcc, 63, v4
	s_nop 1
	v_cndmask_b32_e32 v31, 0, v26, vcc
	v_add_u32_e32 v4, v31, v4
	v_cmp_lt_u32_e64 s[8:9], 31, v4
	s_nop 1
	v_cndmask_b32_e64 v31, 0, v27, s[8:9]
	v_add_u32_e32 v4, v31, v4
	v_cmp_lt_u32_e64 s[10:11], 31, v4
	s_nop 1
	v_cndmask_b32_e64 v31, 0, v27, s[10:11]
	v_add_u32_e32 v31, v31, v4
	v_and_b32_e32 v4, 0x7fffff, v13
	v_or_b32_e32 v44, 0x800000, v4
	v_mad_u64_u32 v[32:33], s[12:13], v44, s36, 0
	v_mov_b32_e32 v4, v33
	v_mad_u64_u32 v[34:35], s[12:13], v44, s37, v[4:5]
	v_mov_b32_e32 v4, v35
	v_mad_u64_u32 v[36:37], s[12:13], v44, s48, v[4:5]
	v_mov_b32_e32 v4, v37
	v_mad_u64_u32 v[38:39], s[12:13], v44, s49, v[4:5]
	v_mov_b32_e32 v4, v39
	v_mad_u64_u32 v[40:41], s[12:13], v44, s50, v[4:5]
	v_mov_b32_e32 v4, v41
	v_mad_u64_u32 v[42:43], s[12:13], v44, s51, v[4:5]
	v_mov_b32_e32 v4, v43
	v_mad_u64_u32 v[44:45], s[12:13], v44, s52, v[4:5]
	v_cndmask_b32_e32 v33, v42, v38, vcc
	v_cndmask_b32_e32 v4, v44, v40, vcc
	v_cndmask_b32_e32 v37, v45, v42, vcc
	v_cndmask_b32_e64 v35, v4, v33, s[8:9]
	v_cndmask_b32_e64 v4, v37, v4, s[8:9]
	v_cndmask_b32_e32 v37, v40, v36, vcc
	v_cndmask_b32_e64 v33, v33, v37, s[8:9]
	v_cndmask_b32_e64 v4, v4, v35, s[10:11]
	v_cndmask_b32_e64 v35, v35, v33, s[10:11]
	v_sub_u32_e32 v39, 32, v31
	v_alignbit_b32 v40, v4, v35, v39
	v_cmp_eq_u32_e64 s[12:13], 0, v31
	v_cndmask_b32_e32 v32, v36, v32, vcc
	s_nop 0
	v_cndmask_b32_e64 v31, v40, v4, s[12:13]
	v_cndmask_b32_e32 v4, v38, v34, vcc
	v_cndmask_b32_e64 v34, v37, v4, s[8:9]
	v_cndmask_b32_e64 v33, v33, v34, s[10:11]
	v_alignbit_b32 v37, v35, v33, v39
	v_cndmask_b32_e64 v35, v37, v35, s[12:13]
	v_bfe_u32 v40, v31, 29, 1
	v_cndmask_b32_e64 v4, v4, v32, s[8:9]
	v_alignbit_b32 v37, v31, v35, 30
	v_sub_u32_e32 v41, 0, v40
	v_cndmask_b32_e64 v4, v34, v4, s[10:11]
	v_xor_b32_e32 v37, v37, v41
	v_alignbit_b32 v32, v33, v4, v39
	v_cndmask_b32_e64 v32, v32, v33, s[12:13]
	v_ffbh_u32_e32 v34, v37
	v_alignbit_b32 v33, v35, v32, 30
	v_min_u32_e32 v34, 32, v34
	v_alignbit_b32 v4, v32, v4, 30
	v_xor_b32_e32 v33, v33, v41
	v_sub_u32_e32 v35, 31, v34
	v_xor_b32_e32 v4, v4, v41
	v_alignbit_b32 v36, v37, v33, v35
	v_alignbit_b32 v4, v33, v4, v35
	v_alignbit_b32 v32, v36, v4, 9
	v_ffbh_u32_e32 v33, v32
	v_min_u32_e32 v33, 32, v33
	v_lshrrev_b32_e32 v38, 29, v31
	v_not_b32_e32 v35, v33
	v_alignbit_b32 v4, v32, v4, v35
	v_lshlrev_b32_e32 v32, 31, v38
	v_or_b32_e32 v35, 0x33000000, v32
	v_add_lshl_u32 v33, v33, v34, 23
	v_lshrrev_b32_e32 v4, 9, v4
	v_sub_u32_e32 v33, v35, v33
	v_or_b32_e32 v32, 0.5, v32
	v_lshlrev_b32_e32 v34, 23, v34
	v_or_b32_e32 v4, v33, v4
	v_lshrrev_b32_e32 v33, 9, v36
	v_sub_u32_e32 v32, v32, v34
	v_or_b32_e32 v32, v33, v32
	v_mul_f32_e32 v33, 0x3fc90fda, v32
	v_fma_f32 v34, v32, s53, -v33
	v_fmac_f32_e32 v34, 0x33a22168, v32
	v_fmac_f32_e32 v34, 0x3fc90fda, v4
	v_lshrrev_b32_e32 v31, 30, v31
	v_add_f32_e32 v4, v33, v34
	v_add_u32_e32 v31, v40, v31
